# P2a S2a Gram epilogue: 16 per-element gating-row LDS reads batched into one prefetch after the MFMAs (both variants)
# baseline (speedup 1.0000x reference)
.LBB0_264:
	v_and_b32_e32 v109, 31, v107
	v_lshrrev_b32_e32 v110, 5, v100
	s_andn2_b64 vcc, exec, s[4:5]
	v_lshrrev_b32_e32 v111, 2, v107
	v_bfe_u32 v112, v107, 2, 2
	s_cbranch_vccnz .LBB0_365
	s_mul_hi_i32 s4, s78, 0x55555556
	s_lshr_b32 s5, s4, 31
	s_add_i32 s4, s4, s5
	s_mul_i32 s4, s4, 3
	s_sub_i32 s26, s78, s4
	s_cmp_gt_i32 s78, 2
	s_cselect_b64 s[4:5], -1, 0
	s_and_b64 vcc, s[4:5], exec
	s_cselect_b32 s4, 0, 0x4000
	s_add_i32 s4, s4, 0
	s_cmp_eq_u32 s26, 0
	s_cselect_b32 s25, 0, 32
	s_cmp_eq_u32 s26, 2
	v_lshlrev_b32_e32 v3, 2, v109
	v_or_b32_e32 v2, s25, v109
	v_and_b32_e32 v10, 12, v3
	s_cselect_b32 s24, 32, 0
	v_or_b32_e32 v13, 2, v110
	v_lshl_add_u32 v11, v2, 8, s4
	v_or_b32_e32 v102, s24, v109
	v_bitop3_b32 v2, v10, v110, v112 bitop3:0x36
	v_bitop3_b32 v13, v10, v13, v112 bitop3:0x36
	v_lshl_add_u32 v12, v102, 8, 0
	v_lshlrev_b32_e32 v2, 4, v2
	v_lshlrev_b32_e32 v13, 4, v13
	v_add_u32_e32 v3, v11, v2
	v_add_u32_e32 v6, v12, v2
	v_add_u32_e32 v14, v11, v13
	v_add_u32_e32 v13, v12, v13
	ds_read_b128 v[2:5], v3
	ds_read_b128 v[6:9], v6 offset:16384
	ds_read_b128 v[114:117], v14
	ds_read_b128 v[122:125], v13 offset:16384
	v_or_b32_e32 v13, 4, v110
	v_bitop3_b32 v13, v10, v13, v112 bitop3:0x36
	v_lshlrev_b32_e32 v13, 4, v13
	v_add_u32_e32 v14, v11, v13
	v_add_u32_e32 v13, v12, v13
	ds_read_b128 v[126:129], v14
	ds_read_b128 v[130:133], v13 offset:16384
	v_or_b32_e32 v13, 6, v110
	v_bitop3_b32 v13, v10, v13, v112 bitop3:0x36
	v_lshlrev_b32_e32 v13, 4, v13
	v_add_u32_e32 v14, v11, v13
	v_add_u32_e32 v13, v12, v13
	ds_read_b128 v[134:137], v14
	ds_read_b128 v[138:141], v13 offset:16384
	v_or_b32_e32 v13, 8, v110
	v_bitop3_b32 v13, v10, v13, v112 bitop3:0x36
	v_lshlrev_b32_e32 v13, 4, v13
	v_add_u32_e32 v14, v11, v13
	v_add_u32_e32 v13, v12, v13
	ds_read_b128 v[142:145], v14
	ds_read_b128 v[146:149], v13 offset:16384
	v_or_b32_e32 v13, 10, v110
	v_bitop3_b32 v13, v10, v13, v112 bitop3:0x36
	v_lshlrev_b32_e32 v13, 4, v13
	v_add_u32_e32 v14, v11, v13
	v_add_u32_e32 v13, v12, v13
	ds_read_b128 v[150:153], v14
	ds_read_b128 v[154:157], v13 offset:16384
	v_or_b32_e32 v13, 12, v110
	v_bitop3_b32 v13, v10, v13, v112 bitop3:0x36
	v_lshlrev_b32_e32 v13, 4, v13
	v_add_u32_e32 v14, v11, v13
	v_add_u32_e32 v13, v12, v13
	ds_read_b128 v[158:161], v14
	ds_read_b128 v[162:165], v13 offset:16384
	v_or_b32_e32 v13, 14, v110
	v_bitop3_b32 v10, v10, v13, v112 bitop3:0x36
	v_lshlrev_b32_e32 v10, 4, v10
	v_add_u32_e32 v11, v11, v10
	v_add_u32_e32 v10, v12, v10
	ds_read_b128 v[166:169], v11
	ds_read_b128 v[170:173], v10 offset:16384
	v_lshl_add_u32 v10, v102, 4, 0
	v_add_u32_e32 v10, 0x1c200, v10
	ds_read_b128 v[94:97], v10
	s_waitcnt lgkmcnt(0)
	v_mfma_f32_32x32x16_bf16 v[2:17], v[2:5], v[6:9], 0
	s_mov_b64 s[4:5], -1
	v_mfma_f32_32x32x16_bf16 v[2:17], v[114:117], v[122:125], v[2:17]
	v_mfma_f32_32x32x16_bf16 v[2:17], v[126:129], v[130:133], v[2:17]
	v_mfma_f32_32x32x16_bf16 v[2:17], v[134:137], v[138:141], v[2:17]
	v_mfma_f32_32x32x16_bf16 v[2:17], v[142:145], v[146:149], v[2:17]
	v_mfma_f32_32x32x16_bf16 v[2:17], v[150:153], v[154:157], v[2:17]
	v_mfma_f32_32x32x16_bf16 v[2:17], v[158:161], v[162:165], v[2:17]
	v_mfma_f32_32x32x16_bf16 v[2:17], v[166:169], v[170:173], v[2:17]
	s_cbranch_vccnz .LBB0_331
	v_lshl_or_b32 v95, v110, 2, s25
	v_lshlrev_b32_e32 v158, 4, v95
	v_add_u32_e32 v158, 0x1c200, v158
	ds_read2_b32 v[126:127], v158 offset0:0 offset1:2
	ds_read2_b32 v[128:129], v158 offset0:4 offset1:6
	ds_read2_b32 v[130:131], v158 offset0:8 offset1:10
	ds_read2_b32 v[132:133], v158 offset0:12 offset1:14
	ds_read2_b32 v[134:135], v158 offset0:32 offset1:34
	ds_read2_b32 v[136:137], v158 offset0:36 offset1:38
	ds_read2_b32 v[138:139], v158 offset0:40 offset1:42
	ds_read2_b32 v[140:141], v158 offset0:44 offset1:46
	ds_read2_b32 v[142:143], v158 offset0:64 offset1:66
	ds_read2_b32 v[144:145], v158 offset0:68 offset1:70
	ds_read2_b32 v[146:147], v158 offset0:72 offset1:74
	ds_read2_b32 v[148:149], v158 offset0:76 offset1:78
	ds_read2_b32 v[150:151], v158 offset0:96 offset1:98
	ds_read2_b32 v[152:153], v158 offset0:100 offset1:102
	ds_read2_b32 v[154:155], v158 offset0:104 offset1:106
	ds_read2_b32 v[156:157], v158 offset0:108 offset1:110
	s_waitcnt lgkmcnt(0)
	v_cmp_lt_u32_e32 vcc, v102, v95
	v_mov_b32_e32 v103, 0
	s_and_saveexec_b64 s[4:5], vcc
	s_cbranch_execz .LBB0_268
	v_lshl_add_u32 v94, v95, 4, 0
	v_add_u32_e32 v94, 0x1c200, v94
	v_sub_f32_e32 v94, v127, v96
	v_exp_f32_e32 v94, v94
	v_mul_f32_e32 v98, v2, v126
	v_mul_f32_e32 v98, v97, v98
	v_mul_f32_e32 v103, v98, v94

.LBB0_270:
	v_or_b32_e32 v103, 1, v95
	v_cmp_le_u32_e32 vcc, v102, v95
	v_mov_b32_e32 v104, 0
	s_and_saveexec_b64 s[4:5], vcc
	s_cbranch_execz .LBB0_272
	v_lshl_add_u32 v104, v103, 4, 0
	v_add_u32_e32 v104, 0x1c200, v104
	v_sub_f32_e32 v104, v129, v96
	v_exp_f32_e32 v104, v104
	v_mul_f32_e32 v105, v3, v128
	v_mul_f32_e32 v105, v97, v105
	v_mul_f32_e32 v104, v105, v104

.LBB0_274:
	v_or_b32_e32 v103, 2, v95
	v_cmp_lt_u32_e32 vcc, v102, v103
	v_mov_b32_e32 v104, 0
	s_and_saveexec_b64 s[22:23], vcc
	s_cbranch_execz .LBB0_276
	v_lshl_add_u32 v104, v103, 4, 0
	v_add_u32_e32 v104, 0x1c200, v104
	v_sub_f32_e32 v104, v131, v96
	v_exp_f32_e32 v104, v104
	v_mul_f32_e32 v105, v4, v130
	v_mul_f32_e32 v105, v97, v105
	v_mul_f32_e32 v104, v105, v104

.LBB0_278:
	v_or_b32_e32 v103, 3, v95
	v_cmp_lt_u32_e32 vcc, v102, v103
	v_mov_b32_e32 v104, 0
	s_and_saveexec_b64 s[22:23], vcc
	s_cbranch_execz .LBB0_280
	v_lshl_add_u32 v104, v103, 4, 0
	v_add_u32_e32 v104, 0x1c200, v104
	v_sub_f32_e32 v104, v133, v96
	v_exp_f32_e32 v104, v104
	v_mul_f32_e32 v105, v5, v132
	v_mul_f32_e32 v105, v97, v105
	v_mul_f32_e32 v104, v105, v104

.LBB0_282:
	v_or_b32_e32 v103, 8, v95
	v_cmp_lt_u32_e32 vcc, v102, v103
	v_mov_b32_e32 v104, 0
	s_and_saveexec_b64 s[22:23], vcc
	s_cbranch_execz .LBB0_284
	v_lshl_add_u32 v104, v103, 4, 0
	v_add_u32_e32 v104, 0x1c200, v104
	v_sub_f32_e32 v104, v135, v96
	v_exp_f32_e32 v104, v104
	v_mul_f32_e32 v105, v6, v134
	v_mul_f32_e32 v105, v97, v105
	v_mul_f32_e32 v104, v105, v104

.LBB0_286:
	v_or_b32_e32 v103, 9, v95
	v_cmp_lt_u32_e32 vcc, v102, v103
	v_mov_b32_e32 v104, 0
	s_and_saveexec_b64 s[22:23], vcc
	s_cbranch_execz .LBB0_288
	v_lshl_add_u32 v104, v103, 4, 0
	v_add_u32_e32 v104, 0x1c200, v104
	v_sub_f32_e32 v104, v137, v96
	v_exp_f32_e32 v104, v104
	v_mul_f32_e32 v105, v7, v136
	v_mul_f32_e32 v105, v97, v105
	v_mul_f32_e32 v104, v105, v104

.LBB0_290:
	v_or_b32_e32 v103, 10, v95
	v_cmp_lt_u32_e32 vcc, v102, v103
	v_mov_b32_e32 v104, 0
	s_and_saveexec_b64 s[22:23], vcc
	s_cbranch_execz .LBB0_292
	v_lshl_add_u32 v104, v103, 4, 0
	v_add_u32_e32 v104, 0x1c200, v104
	v_sub_f32_e32 v104, v139, v96
	v_exp_f32_e32 v104, v104
	v_mul_f32_e32 v105, v8, v138
	v_mul_f32_e32 v105, v97, v105
	v_mul_f32_e32 v104, v105, v104

.LBB0_294:
	v_or_b32_e32 v103, 11, v95
	v_cmp_lt_u32_e32 vcc, v102, v103
	v_mov_b32_e32 v104, 0
	s_and_saveexec_b64 s[22:23], vcc
	s_cbranch_execz .LBB0_296
	v_lshl_add_u32 v104, v103, 4, 0
	v_add_u32_e32 v104, 0x1c200, v104
	v_sub_f32_e32 v104, v141, v96
	v_exp_f32_e32 v104, v104
	v_mul_f32_e32 v105, v9, v140
	v_mul_f32_e32 v105, v97, v105
	v_mul_f32_e32 v104, v105, v104

.LBB0_298:
	v_or_b32_e32 v103, 16, v95
	v_cmp_lt_u32_e32 vcc, v102, v103
	v_mov_b32_e32 v104, 0
	s_and_saveexec_b64 s[22:23], vcc
	s_cbranch_execz .LBB0_300
	v_lshl_add_u32 v104, v103, 4, 0
	v_add_u32_e32 v104, 0x1c200, v104
	v_sub_f32_e32 v104, v143, v96
	v_exp_f32_e32 v104, v104
	v_mul_f32_e32 v105, v10, v142
	v_mul_f32_e32 v105, v97, v105
	v_mul_f32_e32 v104, v105, v104

.LBB0_302:
	v_or_b32_e32 v103, 17, v95
	v_cmp_lt_u32_e32 vcc, v102, v103
	v_mov_b32_e32 v104, 0
	s_and_saveexec_b64 s[22:23], vcc
	s_cbranch_execz .LBB0_304
	v_lshl_add_u32 v104, v103, 4, 0
	v_add_u32_e32 v104, 0x1c200, v104
	v_sub_f32_e32 v104, v145, v96
	v_exp_f32_e32 v104, v104
	v_mul_f32_e32 v105, v11, v144
	v_mul_f32_e32 v105, v97, v105
	v_mul_f32_e32 v104, v105, v104

.LBB0_306:
	v_or_b32_e32 v103, 18, v95
	v_cmp_lt_u32_e32 vcc, v102, v103
	v_mov_b32_e32 v104, 0
	s_and_saveexec_b64 s[22:23], vcc
	s_cbranch_execz .LBB0_308
	v_lshl_add_u32 v104, v103, 4, 0
	v_add_u32_e32 v104, 0x1c200, v104
	v_sub_f32_e32 v104, v147, v96
	v_exp_f32_e32 v104, v104
	v_mul_f32_e32 v105, v12, v146
	v_mul_f32_e32 v105, v97, v105
	v_mul_f32_e32 v104, v105, v104

.LBB0_310:
	v_or_b32_e32 v103, 19, v95
	v_cmp_lt_u32_e32 vcc, v102, v103
	v_mov_b32_e32 v104, 0
	s_and_saveexec_b64 s[22:23], vcc
	s_cbranch_execz .LBB0_312
	v_lshl_add_u32 v104, v103, 4, 0
	v_add_u32_e32 v104, 0x1c200, v104
	v_sub_f32_e32 v104, v149, v96
	v_exp_f32_e32 v104, v104
	v_mul_f32_e32 v105, v13, v148
	v_mul_f32_e32 v105, v97, v105
	v_mul_f32_e32 v104, v105, v104

.LBB0_314:
	v_or_b32_e32 v103, 24, v95
	v_cmp_lt_u32_e32 vcc, v102, v103
	v_mov_b32_e32 v104, 0
	s_and_saveexec_b64 s[22:23], vcc
	s_cbranch_execz .LBB0_316
	v_lshl_add_u32 v104, v103, 4, 0
	v_add_u32_e32 v104, 0x1c200, v104
	v_sub_f32_e32 v104, v151, v96
	v_exp_f32_e32 v104, v104
	v_mul_f32_e32 v105, v14, v150
	v_mul_f32_e32 v105, v97, v105
	v_mul_f32_e32 v104, v105, v104

.LBB0_318:
	v_or_b32_e32 v103, 25, v95
	v_cmp_lt_u32_e32 vcc, v102, v103
	v_mov_b32_e32 v104, 0
	s_and_saveexec_b64 s[22:23], vcc
	s_cbranch_execz .LBB0_320
	v_lshl_add_u32 v104, v103, 4, 0
	v_add_u32_e32 v104, 0x1c200, v104
	v_sub_f32_e32 v104, v153, v96
	v_exp_f32_e32 v104, v104
	v_mul_f32_e32 v105, v15, v152
	v_mul_f32_e32 v105, v97, v105
	v_mul_f32_e32 v104, v105, v104

.LBB0_322:
	v_or_b32_e32 v103, 26, v95
	v_cmp_lt_u32_e32 vcc, v102, v103
	v_mov_b32_e32 v104, 0
	s_and_saveexec_b64 s[22:23], vcc
	s_cbranch_execz .LBB0_324
	v_lshl_add_u32 v104, v103, 4, 0
	v_add_u32_e32 v104, 0x1c200, v104
	v_sub_f32_e32 v104, v155, v96
	v_exp_f32_e32 v104, v104
	v_mul_f32_e32 v105, v16, v154
	v_mul_f32_e32 v105, v97, v105
	v_mul_f32_e32 v104, v105, v104

.LBB0_326:
	v_or_b32_e32 v95, 27, v95
	v_cmp_lt_u32_e32 vcc, v102, v95
	v_mov_b32_e32 v103, 0
	s_and_saveexec_b64 s[22:23], vcc
	s_cbranch_execz .LBB0_328
	v_lshl_add_u32 v103, v95, 4, 0
	v_add_u32_e32 v103, 0x1c200, v103
	v_sub_f32_e32 v103, v157, v96
	v_exp_f32_e32 v103, v103
	v_mul_f32_e32 v104, v17, v156
	v_mul_f32_e32 v104, v97, v104
	v_mul_f32_e32 v103, v104, v103

.LBB0_331:
	s_and_b64 vcc, exec, s[4:5]
	s_cbranch_vccz .LBB0_365
	v_lshlrev_b32_e32 v104, 2, v110
	v_or_b32_e32 v103, s25, v104
	v_lshlrev_b32_e32 v158, 4, v103
	v_add_u32_e32 v158, 0x1c200, v158
	ds_read_b64 v[126:127], v158 offset:4
	ds_read_b64 v[128:129], v158 offset:20
	ds_read_b64 v[130:131], v158 offset:36
	ds_read_b64 v[132:133], v158 offset:52
	ds_read_b64 v[134:135], v158 offset:132
	ds_read_b64 v[136:137], v158 offset:148
	ds_read_b64 v[138:139], v158 offset:164
	ds_read_b64 v[140:141], v158 offset:180
	ds_read_b64 v[142:143], v158 offset:260
	ds_read_b64 v[144:145], v158 offset:276
	ds_read_b64 v[146:147], v158 offset:292
	ds_read_b64 v[148:149], v158 offset:308
	ds_read_b64 v[150:151], v158 offset:388
	ds_read_b64 v[152:153], v158 offset:404
	ds_read_b64 v[154:155], v158 offset:420
	ds_read_b64 v[156:157], v158 offset:436
	s_waitcnt lgkmcnt(0)
	v_cmp_le_u32_e32 vcc, v102, v103
	v_mov_b32_e32 v94, 0
	v_mov_b32_e32 v95, 0
	s_and_saveexec_b64 s[4:5], vcc
	s_cbranch_execz .LBB0_334
	v_lshl_add_u32 v95, v103, 4, 0
	v_add_u32_e32 v95, 0x1c200, v95
	v_sub_f32_e32 v95, v127, v96
	v_exp_f32_e32 v95, v95
	v_mul_f32_e32 v2, v2, v126
	v_mul_f32_e32 v2, v97, v2
	v_mul_f32_e32 v2, v2, v95
	v_cvt_pk_bf16_f32 v95, v2, s0
.LBB0_334:
	s_or_b64 exec, exec, s[4:5]
	s_nop 0
	v_lshlrev_b32_e32 v2, 1, v109
	v_and_b32_e32 v98, 3, v107
	v_and_or_b32 v2, v2, 24, s24
	v_and_or_b32 v98, v111, 4, v98
	v_lshrrev_b32_e32 v105, 3, v2
	v_lshlrev_b32_e32 v114, 1, v98
	v_xor_b32_e32 v2, v105, v104
	v_lshl_or_b32 v2, v2, 4, v114
	v_lshlrev_b32_e32 v98, 7, v103
	v_lshl_add_u64 v[116:117], s[20:21], 0, v[98:99]
	v_mov_b32_e32 v98, v2
	v_lshl_add_u64 v[116:117], v[116:117], 0, v[98:99]
	global_store_short v[116:117], v95, off
	v_or_b32_e32 v95, 1, v103
	v_cmp_le_u32_e32 vcc, v102, v95
	s_and_saveexec_b64 s[4:5], vcc
	s_cbranch_execz .LBB0_336
	v_lshl_add_u32 v2, v95, 4, 0
	v_add_u32_e32 v2, 0x1c200, v2
	v_sub_f32_e32 v2, v129, v96
	v_exp_f32_e32 v2, v2
	v_mul_f32_e32 v3, v3, v128
	v_mul_f32_e32 v3, v97, v3
	v_mul_f32_e32 v2, v3, v2
	v_cvt_pk_bf16_f32 v94, v2, s0
.LBB0_336:
	s_or_b64 exec, exec, s[4:5]
	v_bitop3_b32 v2, v105, v104, 1 bitop3:0x1e
	v_lshlrev_b32_e32 v116, 7, v95
	v_mov_b32_e32 v117, v99
	v_lshl_or_b32 v2, v2, 4, v114
	v_lshl_add_u64 v[116:117], s[20:21], 0, v[116:117]
	v_mov_b32_e32 v3, v99
	v_lshl_add_u64 v[116:117], v[116:117], 0, v[2:3]
	v_or_b32_e32 v95, 2, v103
	global_store_short v[116:117], v94, off
	v_cmp_le_u32_e32 vcc, v102, v95
	v_mov_b32_e32 v115, 0
	v_mov_b32_e32 v116, 0
	s_and_saveexec_b64 s[4:5], vcc
	s_cbranch_execz .LBB0_338
	v_lshl_add_u32 v94, v95, 4, 0
	v_add_u32_e32 v94, 0x1c200, v94
	v_sub_f32_e32 v94, v131, v96
	v_exp_f32_e32 v94, v94
	v_mul_f32_e32 v4, v4, v130
	v_mul_f32_e32 v4, v97, v4
	v_mul_f32_e32 v4, v4, v94
	v_cvt_pk_bf16_f32 v116, v4, s0
.LBB0_338:
	s_or_b64 exec, exec, s[4:5]
	v_bitop3_b32 v4, v105, v104, 2 bitop3:0x1e
	v_lshlrev_b32_e32 v122, 7, v95
	v_mov_b32_e32 v123, v99
	v_lshl_or_b32 v94, v4, 4, v114
	v_lshl_add_u64 v[122:123], s[20:21], 0, v[122:123]
	v_mov_b32_e32 v95, v99
	v_lshl_add_u64 v[122:123], v[122:123], 0, v[94:95]
	global_store_short v[122:123], v116, off
	v_or_b32_e32 v116, 3, v103
	v_cmp_le_u32_e32 vcc, v102, v116
	s_and_saveexec_b64 s[4:5], vcc
	s_cbranch_execz .LBB0_340
	v_lshl_add_u32 v4, v116, 4, 0
	v_add_u32_e32 v4, 0x1c200, v4
	v_sub_f32_e32 v4, v133, v96
	v_exp_f32_e32 v4, v4
	v_mul_f32_e32 v5, v5, v132
	v_mul_f32_e32 v5, v97, v5
	v_mul_f32_e32 v4, v5, v4
	v_cvt_pk_bf16_f32 v115, v4, s0
.LBB0_340:
	s_or_b64 exec, exec, s[4:5]
	v_bitop3_b32 v4, v105, v104, 3 bitop3:0x1e
	v_lshlrev_b32_e32 v104, 7, v116
	v_mov_b32_e32 v105, v99
	v_lshl_or_b32 v4, v4, 4, v114
	v_lshl_add_u64 v[104:105], s[20:21], 0, v[104:105]
	v_mov_b32_e32 v5, v99
	v_lshl_add_u64 v[104:105], v[104:105], 0, v[4:5]
	global_store_short v[104:105], v115, off
	v_or_b32_e32 v105, 8, v103
	v_cmp_le_u32_e32 vcc, v102, v105
	v_mov_b32_e32 v104, 0
	v_mov_b32_e32 v114, 0
	s_and_saveexec_b64 s[4:5], vcc
	s_cbranch_execz .LBB0_342
	v_lshl_add_u32 v114, v105, 4, 0
	v_add_u32_e32 v114, 0x1c200, v114
	v_sub_f32_e32 v114, v135, v96
	v_exp_f32_e32 v114, v114
	v_mul_f32_e32 v6, v6, v134
	v_mul_f32_e32 v6, v97, v6
	v_mul_f32_e32 v6, v6, v114
	v_cvt_pk_bf16_f32 v114, v6, s0
.LBB0_342:
	s_or_b64 exec, exec, s[4:5]
	v_lshlrev_b32_e32 v116, 7, v105
	v_mov_b32_e32 v117, v99
	v_lshl_add_u64 v[116:117], s[20:21], 0, v[116:117]
	v_or_b32_e32 v6, 9, v103
	v_lshl_add_u64 v[116:117], v[116:117], 0, v[98:99]
	v_cmp_le_u32_e32 vcc, v102, v6
	global_store_short v[116:117], v114, off
	s_and_saveexec_b64 s[4:5], vcc
	s_cbranch_execz .LBB0_344
	v_lshl_add_u32 v104, v6, 4, 0
	v_add_u32_e32 v104, 0x1c200, v104
	v_sub_f32_e32 v104, v137, v96
	v_exp_f32_e32 v104, v104
	v_mul_f32_e32 v7, v7, v136
	v_mul_f32_e32 v7, v97, v7
	v_mul_f32_e32 v7, v7, v104
	v_cvt_pk_bf16_f32 v104, v7, s0
.LBB0_344:
	s_or_b64 exec, exec, s[4:5]
	v_lshlrev_b32_e32 v6, 7, v6
	v_mov_b32_e32 v7, v99
	v_lshl_add_u64 v[6:7], s[20:21], 0, v[6:7]
	v_lshl_add_u64 v[6:7], v[6:7], 0, v[2:3]
	global_store_short v[6:7], v104, off
	v_or_b32_e32 v7, 10, v103
	v_cmp_le_u32_e32 vcc, v102, v7
	v_mov_b32_e32 v6, 0
	v_mov_b32_e32 v104, 0
	s_and_saveexec_b64 s[4:5], vcc
	s_cbranch_execz .LBB0_346
	v_lshl_add_u32 v104, v7, 4, 0
	v_add_u32_e32 v104, 0x1c200, v104
	v_sub_f32_e32 v104, v139, v96
	v_exp_f32_e32 v104, v104
	v_mul_f32_e32 v8, v8, v138
	v_mul_f32_e32 v8, v97, v8
	v_mul_f32_e32 v8, v8, v104
	v_cvt_pk_bf16_f32 v104, v8, s0
.LBB0_346:
	s_or_b64 exec, exec, s[4:5]
	v_lshlrev_b32_e32 v114, 7, v7
	v_mov_b32_e32 v115, v99
	v_lshl_add_u64 v[114:115], s[20:21], 0, v[114:115]
	v_or_b32_e32 v7, 11, v103
	v_lshl_add_u64 v[114:115], v[114:115], 0, v[94:95]
	v_cmp_le_u32_e32 vcc, v102, v7
	global_store_short v[114:115], v104, off
	s_and_saveexec_b64 s[4:5], vcc
	s_cbranch_execz .LBB0_348
	v_lshl_add_u32 v6, v7, 4, 0
	v_add_u32_e32 v6, 0x1c200, v6
	v_sub_f32_e32 v6, v141, v96
	v_exp_f32_e32 v6, v6
	v_mul_f32_e32 v8, v9, v140
	v_mul_f32_e32 v8, v97, v8
	v_mul_f32_e32 v6, v8, v6
	v_cvt_pk_bf16_f32 v6, v6, s0
.LBB0_348:
	s_or_b64 exec, exec, s[4:5]
	v_lshlrev_b32_e32 v8, 7, v7
	v_mov_b32_e32 v9, v99
	v_lshl_add_u64 v[8:9], s[20:21], 0, v[8:9]
	v_lshl_add_u64 v[8:9], v[8:9], 0, v[4:5]
	v_or_b32_e32 v7, 16, v103
	global_store_short v[8:9], v6, off
	v_cmp_le_u32_e32 vcc, v102, v7
	v_mov_b32_e32 v6, 0
	v_mov_b32_e32 v8, 0
	s_and_saveexec_b64 s[4:5], vcc
	s_cbranch_execz .LBB0_350
	v_lshl_add_u32 v8, v7, 4, 0
	v_add_u32_e32 v8, 0x1c200, v8
	v_sub_f32_e32 v8, v143, v96
	v_exp_f32_e32 v8, v8
	v_mul_f32_e32 v9, v10, v142
	v_mul_f32_e32 v9, v97, v9
	v_mul_f32_e32 v8, v9, v8
	v_cvt_pk_bf16_f32 v8, v8, s0
.LBB0_350:
	s_or_b64 exec, exec, s[4:5]
	v_lshlrev_b32_e32 v104, 7, v7
	v_mov_b32_e32 v105, v99
	v_lshl_add_u64 v[104:105], s[20:21], 0, v[104:105]
	v_or_b32_e32 v7, 17, v103
	v_lshl_add_u64 v[104:105], v[104:105], 0, v[98:99]
	v_cmp_le_u32_e32 vcc, v102, v7
	global_store_short v[104:105], v8, off
	s_and_saveexec_b64 s[4:5], vcc
	s_cbranch_execz .LBB0_352
	v_lshl_add_u32 v6, v7, 4, 0
	v_add_u32_e32 v6, 0x1c200, v6
	v_sub_f32_e32 v6, v145, v96
	v_exp_f32_e32 v6, v6
	v_mul_f32_e32 v8, v11, v144
	v_mul_f32_e32 v8, v97, v8
	v_mul_f32_e32 v6, v8, v6
	v_cvt_pk_bf16_f32 v6, v6, s0
.LBB0_352:
	s_or_b64 exec, exec, s[4:5]
	v_lshlrev_b32_e32 v8, 7, v7
	v_mov_b32_e32 v9, v99
	v_lshl_add_u64 v[8:9], s[20:21], 0, v[8:9]
	v_lshl_add_u64 v[8:9], v[8:9], 0, v[2:3]
	v_or_b32_e32 v7, 18, v103
	global_store_short v[8:9], v6, off
	v_cmp_le_u32_e32 vcc, v102, v7
	v_mov_b32_e32 v6, 0
	v_mov_b32_e32 v8, 0
	s_and_saveexec_b64 s[4:5], vcc
	s_cbranch_execz .LBB0_354
	v_lshl_add_u32 v8, v7, 4, 0
	v_add_u32_e32 v8, 0x1c200, v8
	v_sub_f32_e32 v8, v147, v96
	v_exp_f32_e32 v8, v8
	v_mul_f32_e32 v146, v12, v146
	v_mul_f32_e32 v146, v97, v146
	v_mul_f32_e32 v8, v146, v8
	v_cvt_pk_bf16_f32 v8, v8, s0
.LBB0_354:
	s_or_b64 exec, exec, s[4:5]
	v_lshlrev_b32_e32 v10, 7, v7
	v_mov_b32_e32 v11, v99
	v_lshl_add_u64 v[10:11], s[20:21], 0, v[10:11]
	v_or_b32_e32 v7, 19, v103
	v_lshl_add_u64 v[10:11], v[10:11], 0, v[94:95]
	v_cmp_le_u32_e32 vcc, v102, v7
	global_store_short v[10:11], v8, off
	s_and_saveexec_b64 s[4:5], vcc
	s_cbranch_execz .LBB0_356
	v_lshl_add_u32 v6, v7, 4, 0
	v_add_u32_e32 v6, 0x1c200, v6
	v_sub_f32_e32 v6, v149, v96
	v_exp_f32_e32 v6, v6
	v_mul_f32_e32 v8, v13, v148
	v_mul_f32_e32 v8, v97, v8
	v_mul_f32_e32 v6, v8, v6
	v_cvt_pk_bf16_f32 v6, v6, s0
.LBB0_356:
	s_or_b64 exec, exec, s[4:5]
	v_lshlrev_b32_e32 v8, 7, v7
	v_mov_b32_e32 v9, v99
	v_lshl_add_u64 v[8:9], s[20:21], 0, v[8:9]
	v_lshl_add_u64 v[8:9], v[8:9], 0, v[4:5]
	v_or_b32_e32 v7, 24, v103
	global_store_short v[8:9], v6, off
	v_cmp_le_u32_e32 vcc, v102, v7
	v_mov_b32_e32 v6, 0
	v_mov_b32_e32 v8, 0
	s_and_saveexec_b64 s[4:5], vcc
	s_cbranch_execz .LBB0_358
	v_lshl_add_u32 v8, v7, 4, 0
	v_add_u32_e32 v8, 0x1c200, v8
	v_sub_f32_e32 v8, v151, v96
	v_exp_f32_e32 v8, v8
	v_mul_f32_e32 v150, v14, v150
	v_mul_f32_e32 v150, v97, v150
	v_mul_f32_e32 v8, v150, v8
	v_cvt_pk_bf16_f32 v8, v8, s0
.LBB0_358:
	s_or_b64 exec, exec, s[4:5]
	v_lshlrev_b32_e32 v10, 7, v7
	v_mov_b32_e32 v11, v99
	v_lshl_add_u64 v[10:11], s[20:21], 0, v[10:11]
	v_or_b32_e32 v7, 25, v103
	v_lshl_add_u64 v[10:11], v[10:11], 0, v[98:99]
	v_cmp_le_u32_e32 vcc, v102, v7
	global_store_short v[10:11], v8, off
	s_and_saveexec_b64 s[4:5], vcc
	s_cbranch_execz .LBB0_360
	v_lshl_add_u32 v6, v7, 4, 0
	v_add_u32_e32 v6, 0x1c200, v6
	v_sub_f32_e32 v6, v153, v96
	v_exp_f32_e32 v6, v6
	v_mul_f32_e32 v8, v15, v152
	v_mul_f32_e32 v8, v97, v8
	v_mul_f32_e32 v6, v8, v6
	v_cvt_pk_bf16_f32 v6, v6, s0
.LBB0_360:
	s_or_b64 exec, exec, s[4:5]
	v_lshlrev_b32_e32 v98, 7, v7
	v_lshl_add_u64 v[8:9], s[20:21], 0, v[98:99]
	v_lshl_add_u64 v[2:3], v[8:9], 0, v[2:3]
	global_store_short v[2:3], v6, off
	v_or_b32_e32 v3, 26, v103
	v_cmp_le_u32_e32 vcc, v102, v3
	v_mov_b32_e32 v2, 0
	v_mov_b32_e32 v6, 0
	s_and_saveexec_b64 s[4:5], vcc
	s_cbranch_execz .LBB0_362
	v_lshl_add_u32 v6, v3, 4, 0
	v_add_u32_e32 v6, 0x1c200, v6
	v_sub_f32_e32 v6, v155, v96
	v_exp_f32_e32 v6, v6
	v_mul_f32_e32 v154, v16, v154
	v_mul_f32_e32 v154, v97, v154
	v_mul_f32_e32 v6, v154, v6
	v_cvt_pk_bf16_f32 v6, v6, s0
.LBB0_362:
	s_or_b64 exec, exec, s[4:5]
	v_lshlrev_b32_e32 v98, 7, v3
	v_lshl_add_u64 v[8:9], s[20:21], 0, v[98:99]
	v_or_b32_e32 v3, 27, v103
	v_lshl_add_u64 v[8:9], v[8:9], 0, v[94:95]
	v_cmp_le_u32_e32 vcc, v102, v3
	global_store_short v[8:9], v6, off
	s_and_saveexec_b64 s[4:5], vcc
	s_cbranch_execz .LBB0_364
	v_lshl_add_u32 v2, v3, 4, 0
	v_add_u32_e32 v2, 0x1c200, v2
	v_sub_f32_e32 v2, v157, v96
	v_exp_f32_e32 v2, v2
	v_mul_f32_e32 v6, v17, v156
	v_mul_f32_e32 v6, v97, v6
	v_mul_f32_e32 v2, v6, v2
	v_cvt_pk_bf16_f32 v2, v2, s0
